# baseline (speedup 1.0000x reference)
.LBB2_10:
	s_or_b64 exec, exec, s[10:11]
	v_mov_b32_e32 v52, 0x7bff7bff
	v_mov_b32_e32 v99, 0x7bff7bff
	v_mov_b32_e32 v98, 0x7bff7bff
	v_mov_b32_e32 v103, 0x7bff7bff
	v_mov_b32_e32 v100, 0xfbfffbff
	v_mov_b32_e32 v101, 0xfbfffbff
	v_mov_b32_e32 v105, 0xfbfffbff
	v_mov_b32_e32 v104, 0xfbfffbff
	v_mov_b64_e32 v[62:63], 0
	v_mov_b64_e32 v[64:65], 0
	v_mov_b64_e32 v[66:67], 0
	v_mov_b64_e32 v[68:69], 0
	v_mov_b64_e32 v[70:71], 0
	v_mov_b64_e32 v[72:73], 0
	v_mov_b64_e32 v[74:75], 0
	v_mov_b64_e32 v[76:77], 0
	v_cmp_lt_i32_e64 s[10:11], v50, v97
	v_mov_b32_e32 v91, v97
	v_and_b32_e32 v92, 3, v50
	s_waitcnt lgkmcnt(0)
	v_cndmask_b32_e64 v10, v11, v10, s[10:11]
	v_add_u32_e32 v92, 8, v92
	v_add_u32_e32 v94, -1, v102
	v_cndmask_b32_e64 v81, 0, v10, s[0:1]
	v_cndmask_b32_e64 v93, 0, v78, s[0:1]
	v_lshlrev_b32_e32 v94, 2, v94
	v_add_lshl_u32 v92, v92, v93, 2
	v_cndmask_b32_e64 v94, 0, v94, s[0:1]
	v_add_u32_e32 v93, 16, v92
	v_lshlrev_b32_e32 v81, 7, v81
	v_min_i32_e32 v116, v92, v94
	v_min_i32_e32 v117, v93, v94
	global_load_dword v87, v116, s[24:25]
	global_load_dword v88, v117, s[24:25]
	v_add_u32_e32 v92, 32, v92
	v_add_u32_e32 v93, 32, v93
	v_mov_b32_e32 v89, v81
	v_mov_b32_e32 v90, v81
	s_nop 1
	v_mov_b32_dpp v89, v81 row_shr:4 row_mask:0xf bank_mask:0xa
	v_mov_b32_dpp v90, v81 row_shl:4 row_mask:0xf bank_mask:0x5
	s_mov_b64 s[78:79], 0xff
	v_cmp_gt_i32_e64 s[44:45], v91, 0
	v_cmp_gt_i32_e64 s[46:47], v91, 1
	v_cmp_gt_i32_e64 s[48:49], v91, 2
	v_cmp_gt_i32_e64 s[50:51], v91, 3
	v_cmp_gt_i32_e64 s[52:53], v91, 4
	v_cmp_gt_i32_e64 s[54:55], v91, 5
	v_cmp_gt_i32_e64 s[56:57], v91, 6
	v_cmp_gt_i32_e64 s[58:59], v91, 7
	s_nop 0
	v_or_b32_dpp v79, v89, v56 quad_perm:[0,0,0,0] row_mask:0xf bank_mask:0xf
	v_or_b32_dpp v80, v89, v56 quad_perm:[1,1,1,1] row_mask:0xf bank_mask:0xf
	s_or_b64 exec, s[44:45], s[78:79]
	global_load_dwordx4 v[10:13], v79, s[30:31]
	global_load_dwordx4 v[14:17], v80, s[30:31]
	s_mov_b64 exec, -1
	s_nop 0
	v_or_b32_dpp v79, v89, v56 quad_perm:[2,2,2,2] row_mask:0xf bank_mask:0xf
	v_or_b32_dpp v80, v89, v56 quad_perm:[3,3,3,3] row_mask:0xf bank_mask:0xf
	s_or_b64 exec, s[48:49], s[78:79]
	global_load_dwordx4 v[18:21], v79, s[30:31]
	global_load_dwordx4 v[22:25], v80, s[30:31]
	s_mov_b64 exec, -1
	s_nop 0
	v_or_b32_dpp v79, v90, v56 quad_perm:[0,0,0,0] row_mask:0xf bank_mask:0xf
	v_or_b32_dpp v80, v90, v56 quad_perm:[1,1,1,1] row_mask:0xf bank_mask:0xf
	s_or_b64 exec, s[52:53], s[78:79]
	global_load_dwordx4 v[26:29], v79, s[30:31]
	global_load_dwordx4 v[30:33], v80, s[30:31]
	s_mov_b64 exec, -1
	s_nop 0
	v_or_b32_dpp v79, v90, v56 quad_perm:[2,2,2,2] row_mask:0xf bank_mask:0xf
	v_or_b32_dpp v80, v90, v56 quad_perm:[3,3,3,3] row_mask:0xf bank_mask:0xf
	s_or_b64 exec, s[56:57], s[78:79]
	global_load_dwordx4 v[34:37], v79, s[30:31]
	global_load_dwordx4 v[38:41], v80, s[30:31]
	s_mov_b64 exec, -1
	v_cmp_gt_i32_e64 s[60:61], v91, 8
	s_cmp_lg_u64 s[60:61], 0
	s_cbranch_scc0 .Lpl_last_a0
.Lpl_steady_a0:
	s_waitcnt vmcnt(6)
	v_lshlrev_b32_e32 v89, 7, v87
	v_lshlrev_b32_e32 v90, 7, v88
	v_min_i32_e32 v116, v92, v94
	v_min_i32_e32 v117, v93, v94
	global_load_dword v87, v116, s[24:25]
	global_load_dword v88, v117, s[24:25]
	v_add_u32_e32 v92, 32, v92
	v_add_u32_e32 v93, 32, v93
	v_cmp_gt_i32_e64 s[62:63], v91, 8
	v_cmp_gt_i32_e64 s[64:65], v91, 9
	v_cmp_gt_i32_e64 s[66:67], v91, 10
	v_cmp_gt_i32_e64 s[68:69], v91, 11
	v_cmp_gt_i32_e64 s[70:71], v91, 12
	v_cmp_gt_i32_e64 s[72:73], v91, 13
	v_cmp_gt_i32_e64 s[74:75], v91, 14
	v_cmp_gt_i32_e64 s[76:77], v91, 15
	s_mov_b64 exec, s[44:45]
	v_pk_minimum3_f16 v52, v52, v10, v14
	v_pk_maximum3_f16 v100, v100, v10, v14
	v_pk_minimum3_f16 v99, v99, v11, v15
	v_pk_maximum3_f16 v101, v101, v11, v15
	v_pk_minimum3_f16 v98, v98, v12, v16
	v_pk_maximum3_f16 v105, v105, v12, v16
	v_pk_minimum3_f16 v103, v103, v13, v17
	v_pk_maximum3_f16 v104, v104, v13, v17
	v_pk_mul_f16 v110, v10, v10
	v_mov_b32_e32 v106, v10
	v_pk_mul_f16 v111, v11, v11
	v_mov_b32_e32 v107, v11
	v_pk_mul_f16 v112, v12, v12
	v_mov_b32_e32 v108, v12
	v_pk_mul_f16 v113, v13, v13
	v_mov_b32_e32 v109, v13
	s_mov_b64 exec, s[46:47]
	v_pk_add_f16 v106, v106, v14
	v_pk_fma_f16 v110, v14, v14, v110
	v_pk_add_f16 v107, v107, v15
	v_pk_fma_f16 v111, v15, v15, v111
	v_pk_add_f16 v108, v108, v16
	v_pk_fma_f16 v112, v16, v16, v112
	v_pk_add_f16 v109, v109, v17
	v_pk_fma_f16 v113, v17, v17, v113
	s_mov_b64 exec, -1
	s_nop 0
	v_or_b32_dpp v79, v89, v56 quad_perm:[0,0,0,0] row_mask:0xf bank_mask:0xf
	v_or_b32_dpp v80, v89, v56 quad_perm:[1,1,1,1] row_mask:0xf bank_mask:0xf
	s_or_b64 exec, s[62:63], s[78:79]
	global_load_dwordx4 v[10:13], v79, s[30:31]
	global_load_dwordx4 v[14:17], v80, s[30:31]
	s_mov_b64 exec, -1
	s_waitcnt vmcnt(8)
	s_mov_b64 exec, s[48:49]
	v_pk_minimum3_f16 v52, v52, v18, v22
	v_pk_maximum3_f16 v100, v100, v18, v22
	v_pk_minimum3_f16 v99, v99, v19, v23
	v_pk_maximum3_f16 v101, v101, v19, v23
	v_pk_minimum3_f16 v98, v98, v20, v24
	v_pk_maximum3_f16 v105, v105, v20, v24
	v_pk_minimum3_f16 v103, v103, v21, v25
	v_pk_maximum3_f16 v104, v104, v21, v25
	v_pk_add_f16 v106, v106, v18
	v_pk_fma_f16 v110, v18, v18, v110
	v_pk_add_f16 v107, v107, v19
	v_pk_fma_f16 v111, v19, v19, v111
	v_pk_add_f16 v108, v108, v20
	v_pk_fma_f16 v112, v20, v20, v112
	v_pk_add_f16 v109, v109, v21
	v_pk_fma_f16 v113, v21, v21, v113
	s_mov_b64 exec, s[50:51]
	v_pk_add_f16 v106, v106, v22
	v_pk_fma_f16 v110, v22, v22, v110
	v_pk_add_f16 v107, v107, v23
	v_pk_fma_f16 v111, v23, v23, v111
	v_pk_add_f16 v108, v108, v24
	v_pk_fma_f16 v112, v24, v24, v112
	v_pk_add_f16 v109, v109, v25
	v_pk_fma_f16 v113, v25, v25, v113
	s_mov_b64 exec, -1
	s_nop 0
	v_or_b32_dpp v79, v89, v56 quad_perm:[2,2,2,2] row_mask:0xf bank_mask:0xf
	v_or_b32_dpp v80, v89, v56 quad_perm:[3,3,3,3] row_mask:0xf bank_mask:0xf
	s_or_b64 exec, s[66:67], s[78:79]
	global_load_dwordx4 v[18:21], v79, s[30:31]
	global_load_dwordx4 v[22:25], v80, s[30:31]
	s_mov_b64 exec, -1
	s_waitcnt vmcnt(8)
	s_mov_b64 exec, s[52:53]
	v_pk_minimum3_f16 v52, v52, v26, v30
	v_pk_maximum3_f16 v100, v100, v26, v30
	v_pk_minimum3_f16 v99, v99, v27, v31
	v_pk_maximum3_f16 v101, v101, v27, v31
	v_pk_minimum3_f16 v98, v98, v28, v32
	v_pk_maximum3_f16 v105, v105, v28, v32
	v_pk_minimum3_f16 v103, v103, v29, v33
	v_pk_maximum3_f16 v104, v104, v29, v33
	v_pk_add_f16 v106, v106, v26
	v_pk_fma_f16 v110, v26, v26, v110
	v_pk_add_f16 v107, v107, v27
	v_pk_fma_f16 v111, v27, v27, v111
	v_pk_add_f16 v108, v108, v28
	v_pk_fma_f16 v112, v28, v28, v112
	v_pk_add_f16 v109, v109, v29
	v_pk_fma_f16 v113, v29, v29, v113
	s_mov_b64 exec, s[54:55]
	v_pk_add_f16 v106, v106, v30
	v_pk_fma_f16 v110, v30, v30, v110
	v_pk_add_f16 v107, v107, v31
	v_pk_fma_f16 v111, v31, v31, v111
	v_pk_add_f16 v108, v108, v32
	v_pk_fma_f16 v112, v32, v32, v112
	v_pk_add_f16 v109, v109, v33
	v_pk_fma_f16 v113, v33, v33, v113
	s_mov_b64 exec, -1
	s_nop 0
	v_or_b32_dpp v79, v90, v56 quad_perm:[0,0,0,0] row_mask:0xf bank_mask:0xf
	v_or_b32_dpp v80, v90, v56 quad_perm:[1,1,1,1] row_mask:0xf bank_mask:0xf
	s_or_b64 exec, s[70:71], s[78:79]
	global_load_dwordx4 v[26:29], v79, s[30:31]
	global_load_dwordx4 v[30:33], v80, s[30:31]
	s_mov_b64 exec, -1
	s_waitcnt vmcnt(8)
	s_mov_b64 exec, s[56:57]
	v_pk_minimum3_f16 v52, v52, v34, v38
	v_pk_maximum3_f16 v100, v100, v34, v38
	v_pk_minimum3_f16 v99, v99, v35, v39
	v_pk_maximum3_f16 v101, v101, v35, v39
	v_pk_minimum3_f16 v98, v98, v36, v40
	v_pk_maximum3_f16 v105, v105, v36, v40
	v_pk_minimum3_f16 v103, v103, v37, v41
	v_pk_maximum3_f16 v104, v104, v37, v41
	v_pk_add_f16 v106, v106, v34
	v_pk_fma_f16 v110, v34, v34, v110
	v_pk_add_f16 v107, v107, v35
	v_pk_fma_f16 v111, v35, v35, v111
	v_pk_add_f16 v108, v108, v36
	v_pk_fma_f16 v112, v36, v36, v112
	v_pk_add_f16 v109, v109, v37
	v_pk_fma_f16 v113, v37, v37, v113
	s_mov_b64 exec, s[58:59]
	v_pk_add_f16 v106, v106, v38
	v_pk_fma_f16 v110, v38, v38, v110
	v_pk_add_f16 v107, v107, v39
	v_pk_fma_f16 v111, v39, v39, v111
	v_pk_add_f16 v108, v108, v40
	v_pk_fma_f16 v112, v40, v40, v112
	v_pk_add_f16 v109, v109, v41
	v_pk_fma_f16 v113, v41, v41, v113
	s_mov_b64 exec, -1
	s_nop 0
	v_or_b32_dpp v79, v90, v56 quad_perm:[2,2,2,2] row_mask:0xf bank_mask:0xf
	v_or_b32_dpp v80, v90, v56 quad_perm:[3,3,3,3] row_mask:0xf bank_mask:0xf
	s_or_b64 exec, s[74:75], s[78:79]
	global_load_dwordx4 v[34:37], v79, s[30:31]
	global_load_dwordx4 v[38:41], v80, s[30:31]
	s_mov_b64 exec, -1
	s_mov_b64 exec, s[44:45]
	v_fma_mix_f32 v72, v106, 1.0, v72 op_sel_hi:[1,0,0]
	v_fma_mix_f32 v73, v106, 1.0, v73 op_sel:[1,0,0] op_sel_hi:[1,0,0]
	v_fma_mix_f32 v76, v110, 1.0, v76 op_sel_hi:[1,0,0]
	v_fma_mix_f32 v77, v110, 1.0, v77 op_sel:[1,0,0] op_sel_hi:[1,0,0]
	v_fma_mix_f32 v70, v107, 1.0, v70 op_sel_hi:[1,0,0]
	v_fma_mix_f32 v71, v107, 1.0, v71 op_sel:[1,0,0] op_sel_hi:[1,0,0]
	v_fma_mix_f32 v74, v111, 1.0, v74 op_sel_hi:[1,0,0]
	v_fma_mix_f32 v75, v111, 1.0, v75 op_sel:[1,0,0] op_sel_hi:[1,0,0]
	v_fma_mix_f32 v64, v108, 1.0, v64 op_sel_hi:[1,0,0]
	v_fma_mix_f32 v65, v108, 1.0, v65 op_sel:[1,0,0] op_sel_hi:[1,0,0]
	v_fma_mix_f32 v68, v112, 1.0, v68 op_sel_hi:[1,0,0]
	v_fma_mix_f32 v69, v112, 1.0, v69 op_sel:[1,0,0] op_sel_hi:[1,0,0]
	v_fma_mix_f32 v62, v109, 1.0, v62 op_sel_hi:[1,0,0]
	v_fma_mix_f32 v63, v109, 1.0, v63 op_sel:[1,0,0] op_sel_hi:[1,0,0]
	v_fma_mix_f32 v66, v113, 1.0, v66 op_sel_hi:[1,0,0]
	v_fma_mix_f32 v67, v113, 1.0, v67 op_sel:[1,0,0] op_sel_hi:[1,0,0]
	s_mov_b64 exec, -1
	s_mov_b64 s[44:45], s[62:63]
	s_mov_b64 s[46:47], s[64:65]
	s_mov_b64 s[48:49], s[66:67]
	s_mov_b64 s[50:51], s[68:69]
	s_mov_b64 s[52:53], s[70:71]
	s_mov_b64 s[54:55], s[72:73]
	s_mov_b64 s[56:57], s[74:75]
	s_mov_b64 s[58:59], s[76:77]
	v_add_u32_e32 v91, -8, v91
	v_cmp_gt_i32_e64 s[60:61], v91, 8
	s_cmp_lg_u64 s[60:61], 0
	s_cbranch_scc1 .Lpl_steady_a0

.LBB3_10:
	s_or_b64 exec, exec, s[10:11]
	v_mov_b32_e32 v52, 0x7bff7bff
	v_mov_b32_e32 v99, 0x7bff7bff
	v_mov_b32_e32 v98, 0x7bff7bff
	v_mov_b32_e32 v103, 0x7bff7bff
	v_mov_b32_e32 v100, 0xfbfffbff
	v_mov_b32_e32 v101, 0xfbfffbff
	v_mov_b32_e32 v105, 0xfbfffbff
	v_mov_b32_e32 v104, 0xfbfffbff
	v_mov_b64_e32 v[62:63], 0
	v_mov_b64_e32 v[64:65], 0
	v_mov_b64_e32 v[66:67], 0
	v_mov_b64_e32 v[68:69], 0
	v_mov_b64_e32 v[70:71], 0
	v_mov_b64_e32 v[72:73], 0
	v_mov_b64_e32 v[74:75], 0
	v_mov_b64_e32 v[76:77], 0
	v_cmp_lt_i32_e64 s[10:11], v50, v97
	v_mov_b32_e32 v91, v97
	v_and_b32_e32 v92, 3, v50
	s_waitcnt lgkmcnt(0)
	v_cndmask_b32_e64 v10, v11, v10, s[10:11]
	v_add_u32_e32 v92, 8, v92
	v_add_u32_e32 v94, -1, v102
	v_cndmask_b32_e64 v81, 0, v10, s[0:1]
	v_cndmask_b32_e64 v93, 0, v78, s[0:1]
	v_lshlrev_b32_e32 v94, 2, v94
	v_add_lshl_u32 v92, v92, v93, 2
	v_cndmask_b32_e64 v94, 0, v94, s[0:1]
	v_add_u32_e32 v93, 16, v92
	v_lshlrev_b32_e32 v81, 7, v81
	v_min_i32_e32 v116, v92, v94
	v_min_i32_e32 v117, v93, v94
	global_load_dword v87, v116, s[20:21]
	global_load_dword v88, v117, s[20:21]
	v_add_u32_e32 v92, 32, v92
	v_add_u32_e32 v93, 32, v93
	v_mov_b32_e32 v89, v81
	v_mov_b32_e32 v90, v81
	s_nop 1
	v_mov_b32_dpp v89, v81 row_shr:4 row_mask:0xf bank_mask:0xa
	v_mov_b32_dpp v90, v81 row_shl:4 row_mask:0xf bank_mask:0x5
	s_mov_b64 s[78:79], 0xff
	v_cmp_gt_i32_e64 s[44:45], v91, 0
	v_cmp_gt_i32_e64 s[46:47], v91, 1
	v_cmp_gt_i32_e64 s[48:49], v91, 2
	v_cmp_gt_i32_e64 s[50:51], v91, 3
	v_cmp_gt_i32_e64 s[52:53], v91, 4
	v_cmp_gt_i32_e64 s[54:55], v91, 5
	v_cmp_gt_i32_e64 s[56:57], v91, 6
	v_cmp_gt_i32_e64 s[58:59], v91, 7
	s_nop 0
	v_or_b32_dpp v79, v89, v56 quad_perm:[0,0,0,0] row_mask:0xf bank_mask:0xf
	v_or_b32_dpp v80, v89, v56 quad_perm:[1,1,1,1] row_mask:0xf bank_mask:0xf
	s_or_b64 exec, s[44:45], s[78:79]
	global_load_dwordx4 v[10:13], v79, s[24:25]
	global_load_dwordx4 v[14:17], v80, s[24:25]
	s_mov_b64 exec, -1
	s_nop 0
	v_or_b32_dpp v79, v89, v56 quad_perm:[2,2,2,2] row_mask:0xf bank_mask:0xf
	v_or_b32_dpp v80, v89, v56 quad_perm:[3,3,3,3] row_mask:0xf bank_mask:0xf
	s_or_b64 exec, s[48:49], s[78:79]
	global_load_dwordx4 v[18:21], v79, s[24:25]
	global_load_dwordx4 v[22:25], v80, s[24:25]
	s_mov_b64 exec, -1
	s_nop 0
	v_or_b32_dpp v79, v90, v56 quad_perm:[0,0,0,0] row_mask:0xf bank_mask:0xf
	v_or_b32_dpp v80, v90, v56 quad_perm:[1,1,1,1] row_mask:0xf bank_mask:0xf
	s_or_b64 exec, s[52:53], s[78:79]
	global_load_dwordx4 v[26:29], v79, s[24:25]
	global_load_dwordx4 v[30:33], v80, s[24:25]
	s_mov_b64 exec, -1
	s_nop 0
	v_or_b32_dpp v79, v90, v56 quad_perm:[2,2,2,2] row_mask:0xf bank_mask:0xf
	v_or_b32_dpp v80, v90, v56 quad_perm:[3,3,3,3] row_mask:0xf bank_mask:0xf
	s_or_b64 exec, s[56:57], s[78:79]
	global_load_dwordx4 v[34:37], v79, s[24:25]
	global_load_dwordx4 v[38:41], v80, s[24:25]
	s_mov_b64 exec, -1
	v_cmp_gt_i32_e64 s[60:61], v91, 8
	s_cmp_lg_u64 s[60:61], 0
	s_cbranch_scc0 .Lpl_last_a1
.Lpl_steady_a1:
	s_waitcnt vmcnt(6)
	v_lshlrev_b32_e32 v89, 7, v87
	v_lshlrev_b32_e32 v90, 7, v88
	v_min_i32_e32 v116, v92, v94
	v_min_i32_e32 v117, v93, v94
	global_load_dword v87, v116, s[20:21]
	global_load_dword v88, v117, s[20:21]
	v_add_u32_e32 v92, 32, v92
	v_add_u32_e32 v93, 32, v93
	v_cmp_gt_i32_e64 s[62:63], v91, 8
	v_cmp_gt_i32_e64 s[64:65], v91, 9
	v_cmp_gt_i32_e64 s[66:67], v91, 10
	v_cmp_gt_i32_e64 s[68:69], v91, 11
	v_cmp_gt_i32_e64 s[70:71], v91, 12
	v_cmp_gt_i32_e64 s[72:73], v91, 13
	v_cmp_gt_i32_e64 s[74:75], v91, 14
	v_cmp_gt_i32_e64 s[76:77], v91, 15
	s_mov_b64 exec, s[44:45]
	v_pk_minimum3_f16 v52, v52, v10, v14
	v_pk_maximum3_f16 v100, v100, v10, v14
	v_pk_minimum3_f16 v99, v99, v11, v15
	v_pk_maximum3_f16 v101, v101, v11, v15
	v_pk_minimum3_f16 v98, v98, v12, v16
	v_pk_maximum3_f16 v105, v105, v12, v16
	v_pk_minimum3_f16 v103, v103, v13, v17
	v_pk_maximum3_f16 v104, v104, v13, v17
	v_pk_mul_f16 v110, v10, v10
	v_mov_b32_e32 v106, v10
	v_pk_mul_f16 v111, v11, v11
	v_mov_b32_e32 v107, v11
	v_pk_mul_f16 v112, v12, v12
	v_mov_b32_e32 v108, v12
	v_pk_mul_f16 v113, v13, v13
	v_mov_b32_e32 v109, v13
	s_mov_b64 exec, s[46:47]
	v_pk_add_f16 v106, v106, v14
	v_pk_fma_f16 v110, v14, v14, v110
	v_pk_add_f16 v107, v107, v15
	v_pk_fma_f16 v111, v15, v15, v111
	v_pk_add_f16 v108, v108, v16
	v_pk_fma_f16 v112, v16, v16, v112
	v_pk_add_f16 v109, v109, v17
	v_pk_fma_f16 v113, v17, v17, v113
	s_mov_b64 exec, -1
	s_nop 0
	v_or_b32_dpp v79, v89, v56 quad_perm:[0,0,0,0] row_mask:0xf bank_mask:0xf
	v_or_b32_dpp v80, v89, v56 quad_perm:[1,1,1,1] row_mask:0xf bank_mask:0xf
	s_or_b64 exec, s[62:63], s[78:79]
	global_load_dwordx4 v[10:13], v79, s[24:25]
	global_load_dwordx4 v[14:17], v80, s[24:25]
	s_mov_b64 exec, -1
	s_waitcnt vmcnt(8)
	s_mov_b64 exec, s[48:49]
	v_pk_minimum3_f16 v52, v52, v18, v22
	v_pk_maximum3_f16 v100, v100, v18, v22
	v_pk_minimum3_f16 v99, v99, v19, v23
	v_pk_maximum3_f16 v101, v101, v19, v23
	v_pk_minimum3_f16 v98, v98, v20, v24
	v_pk_maximum3_f16 v105, v105, v20, v24
	v_pk_minimum3_f16 v103, v103, v21, v25
	v_pk_maximum3_f16 v104, v104, v21, v25
	v_pk_add_f16 v106, v106, v18
	v_pk_fma_f16 v110, v18, v18, v110
	v_pk_add_f16 v107, v107, v19
	v_pk_fma_f16 v111, v19, v19, v111
	v_pk_add_f16 v108, v108, v20
	v_pk_fma_f16 v112, v20, v20, v112
	v_pk_add_f16 v109, v109, v21
	v_pk_fma_f16 v113, v21, v21, v113
	s_mov_b64 exec, s[50:51]
	v_pk_add_f16 v106, v106, v22
	v_pk_fma_f16 v110, v22, v22, v110
	v_pk_add_f16 v107, v107, v23
	v_pk_fma_f16 v111, v23, v23, v111
	v_pk_add_f16 v108, v108, v24
	v_pk_fma_f16 v112, v24, v24, v112
	v_pk_add_f16 v109, v109, v25
	v_pk_fma_f16 v113, v25, v25, v113
	s_mov_b64 exec, -1
	s_nop 0
	v_or_b32_dpp v79, v89, v56 quad_perm:[2,2,2,2] row_mask:0xf bank_mask:0xf
	v_or_b32_dpp v80, v89, v56 quad_perm:[3,3,3,3] row_mask:0xf bank_mask:0xf
	s_or_b64 exec, s[66:67], s[78:79]
	global_load_dwordx4 v[18:21], v79, s[24:25]
	global_load_dwordx4 v[22:25], v80, s[24:25]
	s_mov_b64 exec, -1
	s_waitcnt vmcnt(8)
	s_mov_b64 exec, s[52:53]
	v_pk_minimum3_f16 v52, v52, v26, v30
	v_pk_maximum3_f16 v100, v100, v26, v30
	v_pk_minimum3_f16 v99, v99, v27, v31
	v_pk_maximum3_f16 v101, v101, v27, v31
	v_pk_minimum3_f16 v98, v98, v28, v32
	v_pk_maximum3_f16 v105, v105, v28, v32
	v_pk_minimum3_f16 v103, v103, v29, v33
	v_pk_maximum3_f16 v104, v104, v29, v33
	v_pk_add_f16 v106, v106, v26
	v_pk_fma_f16 v110, v26, v26, v110
	v_pk_add_f16 v107, v107, v27
	v_pk_fma_f16 v111, v27, v27, v111
	v_pk_add_f16 v108, v108, v28
	v_pk_fma_f16 v112, v28, v28, v112
	v_pk_add_f16 v109, v109, v29
	v_pk_fma_f16 v113, v29, v29, v113
	s_mov_b64 exec, s[54:55]
	v_pk_add_f16 v106, v106, v30
	v_pk_fma_f16 v110, v30, v30, v110
	v_pk_add_f16 v107, v107, v31
	v_pk_fma_f16 v111, v31, v31, v111
	v_pk_add_f16 v108, v108, v32
	v_pk_fma_f16 v112, v32, v32, v112
	v_pk_add_f16 v109, v109, v33
	v_pk_fma_f16 v113, v33, v33, v113
	s_mov_b64 exec, -1
	s_nop 0
	v_or_b32_dpp v79, v90, v56 quad_perm:[0,0,0,0] row_mask:0xf bank_mask:0xf
	v_or_b32_dpp v80, v90, v56 quad_perm:[1,1,1,1] row_mask:0xf bank_mask:0xf
	s_or_b64 exec, s[70:71], s[78:79]
	global_load_dwordx4 v[26:29], v79, s[24:25]
	global_load_dwordx4 v[30:33], v80, s[24:25]
	s_mov_b64 exec, -1
	s_waitcnt vmcnt(8)
	s_mov_b64 exec, s[56:57]
	v_pk_minimum3_f16 v52, v52, v34, v38
	v_pk_maximum3_f16 v100, v100, v34, v38
	v_pk_minimum3_f16 v99, v99, v35, v39
	v_pk_maximum3_f16 v101, v101, v35, v39
	v_pk_minimum3_f16 v98, v98, v36, v40
	v_pk_maximum3_f16 v105, v105, v36, v40
	v_pk_minimum3_f16 v103, v103, v37, v41
	v_pk_maximum3_f16 v104, v104, v37, v41
	v_pk_add_f16 v106, v106, v34
	v_pk_fma_f16 v110, v34, v34, v110
	v_pk_add_f16 v107, v107, v35
	v_pk_fma_f16 v111, v35, v35, v111
	v_pk_add_f16 v108, v108, v36
	v_pk_fma_f16 v112, v36, v36, v112
	v_pk_add_f16 v109, v109, v37
	v_pk_fma_f16 v113, v37, v37, v113
	s_mov_b64 exec, s[58:59]
	v_pk_add_f16 v106, v106, v38
	v_pk_fma_f16 v110, v38, v38, v110
	v_pk_add_f16 v107, v107, v39
	v_pk_fma_f16 v111, v39, v39, v111
	v_pk_add_f16 v108, v108, v40
	v_pk_fma_f16 v112, v40, v40, v112
	v_pk_add_f16 v109, v109, v41
	v_pk_fma_f16 v113, v41, v41, v113
	s_mov_b64 exec, -1
	s_nop 0
	v_or_b32_dpp v79, v90, v56 quad_perm:[2,2,2,2] row_mask:0xf bank_mask:0xf
	v_or_b32_dpp v80, v90, v56 quad_perm:[3,3,3,3] row_mask:0xf bank_mask:0xf
	s_or_b64 exec, s[74:75], s[78:79]
	global_load_dwordx4 v[34:37], v79, s[24:25]
	global_load_dwordx4 v[38:41], v80, s[24:25]
	s_mov_b64 exec, -1
	s_mov_b64 exec, s[44:45]
	v_fma_mix_f32 v72, v106, 1.0, v72 op_sel_hi:[1,0,0]
	v_fma_mix_f32 v73, v106, 1.0, v73 op_sel:[1,0,0] op_sel_hi:[1,0,0]
	v_fma_mix_f32 v76, v110, 1.0, v76 op_sel_hi:[1,0,0]
	v_fma_mix_f32 v77, v110, 1.0, v77 op_sel:[1,0,0] op_sel_hi:[1,0,0]
	v_fma_mix_f32 v70, v107, 1.0, v70 op_sel_hi:[1,0,0]
	v_fma_mix_f32 v71, v107, 1.0, v71 op_sel:[1,0,0] op_sel_hi:[1,0,0]
	v_fma_mix_f32 v74, v111, 1.0, v74 op_sel_hi:[1,0,0]
	v_fma_mix_f32 v75, v111, 1.0, v75 op_sel:[1,0,0] op_sel_hi:[1,0,0]
	v_fma_mix_f32 v64, v108, 1.0, v64 op_sel_hi:[1,0,0]
	v_fma_mix_f32 v65, v108, 1.0, v65 op_sel:[1,0,0] op_sel_hi:[1,0,0]
	v_fma_mix_f32 v68, v112, 1.0, v68 op_sel_hi:[1,0,0]
	v_fma_mix_f32 v69, v112, 1.0, v69 op_sel:[1,0,0] op_sel_hi:[1,0,0]
	v_fma_mix_f32 v62, v109, 1.0, v62 op_sel_hi:[1,0,0]
	v_fma_mix_f32 v63, v109, 1.0, v63 op_sel:[1,0,0] op_sel_hi:[1,0,0]
	v_fma_mix_f32 v66, v113, 1.0, v66 op_sel_hi:[1,0,0]
	v_fma_mix_f32 v67, v113, 1.0, v67 op_sel:[1,0,0] op_sel_hi:[1,0,0]
	s_mov_b64 exec, -1
	s_mov_b64 s[44:45], s[62:63]
	s_mov_b64 s[46:47], s[64:65]
	s_mov_b64 s[48:49], s[66:67]
	s_mov_b64 s[50:51], s[68:69]
	s_mov_b64 s[52:53], s[70:71]
	s_mov_b64 s[54:55], s[72:73]
	s_mov_b64 s[56:57], s[74:75]
	s_mov_b64 s[58:59], s[76:77]
	v_add_u32_e32 v91, -8, v91
	v_cmp_gt_i32_e64 s[60:61], v91, 8
	s_cmp_lg_u64 s[60:61], 0
	s_cbranch_scc1 .Lpl_steady_a1
